# burst priority around QK MFMAs instead of static priority for waves 4-7
# baseline (speedup 1.0000x reference)
.LBB0_692:
	s_mov_b32 s77, s93
	s_add_i32 s58, s36, 0x3400
	s_add_i32 s59, s36, 0x2000
	s_add_i32 s38, s51, s83
	s_lshl_b64 s[8:9], s[76:77], 26
	s_add_u32 s39, s30, s8
	v_writelane_b32 v252, s40, 23
	s_addc_u32 s40, s28, s9
	s_add_u32 s41, s31, s8
	s_addc_u32 s42, s29, s9
	s_add_u32 s43, s35, s8
	s_addc_u32 s44, s34, s9
	s_add_u32 s45, s27, 0x80000
	s_addc_u32 s46, s26, 0
	s_add_u32 s47, s27, 0x3f200000
	s_addc_u32 s48, s26, 0
	s_add_i32 s49, s76, 1
	s_cmp_eq_u32 s76, 3
	s_mov_b32 s8, 0xa000
	s_cselect_b32 s50, 0x6000, s8
	s_lshl_b32 s61, s51, 5
	s_ashr_i32 s8, s61, 31
	s_add_u32 s22, s27, 0x1ae00000
	s_addc_u32 s23, s26, 0
	v_and_b32_e32 v204, 31, v2
	v_and_b32_e32 v9, 16, v2
	v_lshlrev_b32_e32 v10, 2, v2
	s_add_u32 s62, s27, 0x20e00000
	v_lshrrev_b32_e32 v5, 5, v4
	v_mul_u32_u24_e32 v6, 0xd0, v204
	v_lshlrev_b32_e32 v8, 4, v2
	v_and_or_b32 v9, v10, 12, v9
	s_addc_u32 s63, s26, 0
	v_lshl_add_u32 v205, v5, 4, v6
	v_lshlrev_b32_e32 v6, 8, v5
	v_and_b32_e32 v8, 0xc0, v8
	v_lshlrev_b32_e32 v9, 1, v9
	s_add_u32 s51, s27, 0x43200000
	v_and_b32_e32 v7, 15, v2
	v_or3_b32 v206, v6, v8, v9
	s_waitcnt vmcnt(6)
	s_barrier
	v_mov_b32_e32 v189, s8
	v_lshlrev_b32_e32 v6, 3, v5
	s_addc_u32 s52, s26, 0
	v_lshrrev_b32_e32 v2, 1, v2
	v_cmp_gt_u32_e64 s[8:9], 16, v4
	v_lshlrev_b32_e32 v8, 2, v5
	v_mov_b32_e32 v4, v3
	v_mov_b32_e32 v5, v3
	v_and_b32_e32 v178, 24, v2
	s_add_u32 s24, s27, 0x2f200000
	v_mov_b32_e32 v2, v3
	v_mov_b64_e32 v[100:101], v[4:5]
	s_mov_b32 s60, 3
	v_or_b32_e32 v188, s61, v204
	v_lshlrev_b32_e32 v199, 11, v7
	v_mov_b32_e32 v179, v3
	v_lshlrev_b32_e32 v180, 2, v7
	s_addc_u32 s25, s26, 0
	v_or_b32_e32 v207, 59, v8
	v_mov_b32_e32 v102, v3
	v_mov_b32_e32 v103, v3
	v_mov_b32_e32 v104, v3
	v_mov_b32_e32 v105, v3
	v_mov_b32_e32 v106, v3
	v_mov_b32_e32 v107, v3
	v_mov_b32_e32 v108, v3
	v_mov_b32_e32 v109, v3
	v_mov_b32_e32 v110, v3
	v_mov_b32_e32 v111, v3
	v_mov_b32_e32 v112, v3
	v_mov_b32_e32 v113, v3
	v_mov_b32_e32 v114, v3
	v_mov_b32_e32 v115, v3
	v_mov_b32_e32 v116, v3
	v_mov_b32_e32 v117, v3
	v_mov_b32_e32 v118, v3
	v_mov_b32_e32 v119, v3
	v_mov_b32_e32 v120, v3
	v_mov_b32_e32 v121, v3
	v_mov_b32_e32 v122, v3
	v_mov_b32_e32 v123, v3
	v_mov_b32_e32 v124, v3
	v_mov_b32_e32 v125, v3
	v_mov_b32_e32 v126, v3
	v_mov_b32_e32 v127, v3
	v_mov_b32_e32 v128, v3
	v_mov_b32_e32 v129, v3
	v_mov_b32_e32 v130, v3
	v_mov_b32_e32 v131, v3
	v_mov_b32_e32 v132, v3
	v_mov_b32_e32 v133, v3
	v_mov_b64_e32 v[186:187], 0
	s_mov_b32 s64, 0
	v_lshlrev_b32_e32 v190, 1, v6
	v_lshlrev_b32_e32 v192, 1, v8
	v_readlane_b32 s65, v252, 28
	v_readlane_b32 s66, v252, 26
	v_readlane_b32 s67, v252, 18
	s_mov_b32 s69, 0
	s_mov_b32 s70, 0
	v_mov_b64_e32 v[98:99], v[2:3]
	v_mov_b64_e32 v[184:185], 0
	v_mov_b64_e32 v[182:183], 0
	s_mov_b32 s68, 0
	s_mov_b32 s53, 0
	v_xor_b32_e32 v223, 32, v242
	v_lshlrev_b32_e32 v223, 2, v223

.LBB0_719:
	s_mul_i32 s26, s64, 0x5400
	v_add_u32_e32 v2, s26, v205
	s_waitcnt lgkmcnt(3)
	ds_read_b128 v[4:7], v2
	s_waitcnt lgkmcnt(1)
	ds_read_b128 v[8:11], v2 offset:32
	ds_read_b128 v[12:15], v2 offset:6656
	ds_read_b128 v[82:85], v2 offset:6688
	ds_read_b128 v[158:161], v2 offset:64
	ds_read_b128 v[162:165], v2 offset:96
	ds_read_b128 v[86:89], v2 offset:6720
	ds_read_b128 v[90:93], v2 offset:6752
	ds_read_b128 v[194:197], v2 offset:128
	ds_read_b128 v[208:211], v2 offset:160
	ds_read_b128 v[94:97], v2 offset:6784
	ds_read_b128 v[166:169], v2 offset:6816
	v_add_u32_e32 v2, s26, v206
	s_setprio 1
	s_waitcnt lgkmcnt(9)
	v_mfma_f32_32x32x16_bf16 v[66:81], v[12:15], v[134:137], v[50:65]
	s_waitcnt lgkmcnt(8)
	v_mfma_f32_32x32x16_bf16 v[66:81], v[82:85], v[138:141], v[66:81]
	s_waitcnt lgkmcnt(5)
	v_mfma_f32_32x32x16_bf16 v[66:81], v[86:89], v[142:145], v[66:81]
	s_waitcnt lgkmcnt(4)
	v_mfma_f32_32x32x16_bf16 v[66:81], v[90:93], v[146:149], v[66:81]
	s_waitcnt lgkmcnt(1)
	v_mfma_f32_32x32x16_bf16 v[66:81], v[94:97], v[150:153], v[66:81]
	s_waitcnt lgkmcnt(0)
	v_mfma_f32_32x32x16_bf16 v[66:81], v[166:169], v[154:157], v[66:81]
	v_mfma_f32_32x32x16_bf16 v[82:97], v[4:7], v[134:137], v[50:65]
	v_mfma_f32_32x32x16_bf16 v[82:97], v[8:11], v[138:141], v[82:97]
	ds_read_b64_tr_b16 v[174:175], v2 offset:13312
	ds_read_b64_tr_b16 v[176:177], v2 offset:13824
	ds_read_b64_tr_b16 v[170:171], v2 offset:14336
	ds_read_b64_tr_b16 v[172:173], v2 offset:14848
	ds_read_b64_tr_b16 v[166:167], v2 offset:15360
	ds_read_b64_tr_b16 v[168:169], v2 offset:15872
	ds_read_b64_tr_b16 v[8:9], v2 offset:16384
	ds_read_b64_tr_b16 v[10:11], v2 offset:16896
	v_mfma_f32_32x32x16_bf16 v[82:97], v[158:161], v[142:145], v[82:97]
	v_mfma_f32_32x32x16_bf16 v[82:97], v[162:165], v[146:149], v[82:97]
	ds_read_b64_tr_b16 v[162:163], v2 offset:17408
	ds_read_b64_tr_b16 v[164:165], v2 offset:17920
	ds_read_b64_tr_b16 v[158:159], v2 offset:18432
	ds_read_b64_tr_b16 v[160:161], v2 offset:18944
	ds_read_b64_tr_b16 v[12:13], v2 offset:19456
	ds_read_b64_tr_b16 v[14:15], v2 offset:19968
	ds_read_b64_tr_b16 v[4:5], v2 offset:20480
	ds_read_b64_tr_b16 v[6:7], v2 offset:20992
	v_mfma_f32_32x32x16_bf16 v[82:97], v[194:197], v[150:153], v[82:97]
	v_mfma_f32_32x32x16_bf16 v[82:97], v[208:211], v[154:157], v[82:97]
	s_setprio 0
	s_nop 4
	v_max3_f32 v194, v66, v67, v68
	v_max3_f32 v196, v69, v70, v71
	v_max3_f32 v194, v194, v72, v73
	v_max3_f32 v196, v196, v74, v75
	v_max3_f32 v194, v194, v76, v77
	v_max3_f32 v196, v196, v78, v79
	v_max3_f32 v194, v194, v196, v80
	v_max3_f32 v2, v82, v83, v84
	v_max3_f32 v195, v85, v86, v87
	v_max3_f32 v2, v2, v88, v89
	v_max3_f32 v195, v195, v90, v91
	v_max3_f32 v2, v2, v92, v93
	v_max3_f32 v195, v195, v94, v95
	v_max3_f32 v2, v2, v195, v96
	v_max_f32_e32 v195, v97, v81
	v_max3_f32 v2, v2, v194, v195
	ds_bpermute_b32 v194, v223, v2
	s_cmp_lg_u32 s73, 0
	s_waitcnt lgkmcnt(0)
	v_max_f32_e32 v208, v2, v194
	s_cbranch_scc0 .Lmla_f_first
	v_cmp_lt_f32_e32 vcc, s81, v208
	s_cbranch_vccz .LBB0_726
	v_max_f32_e32 v2, v208, v208
	v_max_f32_e32 v2, 0, v2
	s_branch .Lmla_f_resc

.LBB0_851:
	s_mul_i32 s2, s74, 0x4400
	s_add_i32 s6, s2, 0
	v_add_u32_e32 v5, s6, v207
	ds_read_b128 v[6:9], v5 offset:4608
	ds_read_b128 v[10:13], v5
	ds_read_b128 v[14:17], v5 offset:32
	ds_read_b128 v[146:149], v5 offset:4640
	s_cmp_lg_u32 s10, 0
	s_cselect_b64 s[2:3], -1, 0
	s_setprio 1
	s_waitcnt lgkmcnt(2)
	v_mfma_f32_32x32x16_bf16 v[130:145], v[10:13], v[178:181], v[98:113]
	s_and_b64 vcc, exec, s[2:3]
	v_mfma_f32_32x32x16_bf16 v[114:129], v[6:9], v[178:181], v[98:113]
	s_waitcnt lgkmcnt(1)
	v_mfma_f32_32x32x16_bf16 v[130:145], v[14:17], v[182:185], v[130:145]
	s_waitcnt lgkmcnt(0)
	v_mfma_f32_32x32x16_bf16 v[114:129], v[146:149], v[182:185], v[114:129]
	s_setprio 0
	s_nop 9
	v_max3_f32 v2, v130, v131, v132
	v_max3_f32 v8, v133, v134, v135
	v_max3_f32 v6, v114, v115, v116
	v_max3_f32 v7, v117, v118, v119
	v_max3_f32 v2, v2, v136, v137
	v_max3_f32 v8, v8, v138, v139
	v_max3_f32 v6, v6, v120, v121
	v_max3_f32 v7, v7, v122, v123
	v_max3_f32 v2, v2, v140, v141
	v_max3_f32 v8, v8, v142, v143
	v_max3_f32 v6, v6, v124, v125
	v_max3_f32 v7, v7, v126, v127
	v_max3_f32 v2, v2, v8, v144
	v_max3_f32 v6, v6, v7, v128
	v_max_f32_e32 v7, v145, v129
	v_max3_f32 v2, v2, v6, v7
	ds_bpermute_b32 v6, v230, v2
	s_waitcnt lgkmcnt(0)
	v_max_f32_e32 v6, v2, v6
	s_cbranch_vccz .Ldf0_first
	v_cmp_lt_f32_e32 vcc, s11, v6
	s_cbranch_vccz .LBB0_858
	v_max_f32_e32 v2, v6, v6
	v_max_f32_e32 v2, 0, v2
	s_branch .Ldf0_resc

.LBB0_858:
	ds_read_b128 v[6:9], v5 offset:64
	ds_read_b128 v[10:13], v5 offset:96
	ds_read_b128 v[14:17], v5 offset:4672
	ds_read_b128 v[194:197], v5 offset:4704
	s_setprio 1
	s_waitcnt lgkmcnt(3)
	v_mfma_f32_32x32x16_bf16 v[162:177], v[6:9], v[186:189], v[82:97]
	s_and_b64 vcc, exec, s[2:3]
	s_waitcnt lgkmcnt(1)
	v_mfma_f32_32x32x16_bf16 v[146:161], v[14:17], v[186:189], v[82:97]
	v_mfma_f32_32x32x16_bf16 v[162:177], v[10:13], v[190:193], v[162:177]
	s_waitcnt lgkmcnt(0)
	v_mfma_f32_32x32x16_bf16 v[146:161], v[194:197], v[190:193], v[146:161]
	s_setprio 0
	s_nop 9
	v_max3_f32 v2, v162, v163, v164
	v_max3_f32 v7, v165, v166, v167
	v_max3_f32 v5, v146, v147, v148
	v_max3_f32 v6, v149, v150, v151
	v_max3_f32 v2, v2, v168, v169
	v_max3_f32 v7, v7, v170, v171
	v_max3_f32 v5, v5, v152, v153
	v_max3_f32 v6, v6, v154, v155
	v_max3_f32 v2, v2, v172, v173
	v_max3_f32 v7, v7, v174, v175
	v_max3_f32 v5, v5, v156, v157
	v_max3_f32 v6, v6, v158, v159
	v_max3_f32 v2, v2, v7, v176
	v_max3_f32 v5, v5, v6, v160
	v_max_f32_e32 v6, v177, v161
	v_max3_f32 v2, v2, v5, v6
	ds_bpermute_b32 v4, v230, v2
	s_waitcnt lgkmcnt(0)
	v_max_f32_e32 v4, v2, v4
	s_cbranch_vccz .Ldf1_first
	v_cmp_lt_f32_e32 vcc, s11, v4
	s_cbranch_vccz .LBB0_839
	v_max_f32_e32 v2, v4, v4
	v_max_f32_e32 v2, 0, v2
	s_branch .Ldf1_resc
